# nt hint also on P7's last-use loads (XB residual, YP expert outputs) and P3's residual loads
# speedup vs baseline: 1.0191x; 1.0077x over previous
.LBB0_373:
	v_mov_b32_e32 v35, v0
	s_lshl_b32 s4, s57, 8
	v_ashrrev_i32_e32 v34, 2, v35
	v_and_b32_e32 v34, 0xffffffc0, v34
	v_lshl_add_u32 v34, s56, 8, v34
	v_and_b32_e32 v36, 0xc0, v35
	v_and_or_b32 v34, v35, 15, v34
	v_lshrrev_b32_e32 v35, 1, v35
	v_and_b32_e32 v35, 24, v35
	v_or3_b32 v36, v36, s4, v35
	v_ashrrev_i32_e32 v37, 31, v36
	v_lshlrev_b64 v[174:175], 1, v[36:37]
	v_ashrrev_i32_e32 v35, 31, v34
	v_lshl_add_u64 v[36:37], s[16:17], 0, v[174:175]
	v_lshlrev_b64 v[50:51], 11, v[34:35]
	v_lshl_add_u64 v[52:53], v[36:37], 0, v[50:51]
	global_load_dwordx4 v[210:213], v[52:53], off nt
	global_load_dwordx4 v[214:217], v[52:53], off offset:64 nt
	v_or_b32_e32 v52, 16, v34
	v_ashrrev_i32_e32 v53, 31, v52
	v_lshlrev_b64 v[234:235], 11, v[52:53]
	v_lshl_add_u64 v[52:53], v[36:37], 0, v[234:235]
	global_load_dwordx4 v[218:221], v[52:53], off nt
	global_load_dwordx4 v[222:225], v[52:53], off offset:64 nt
	v_or_b32_e32 v58, 32, v34
	v_or_b32_e32 v34, 48, v34
	v_ashrrev_i32_e32 v59, 31, v58
	v_ashrrev_i32_e32 v35, 31, v34
	v_lshlrev_b64 v[186:187], 11, v[58:59]
	v_lshlrev_b64 v[184:185], 11, v[34:35]
	v_lshl_add_u64 v[182:183], v[50:51], 0, s[10:11]
	v_lshl_add_u64 v[180:181], v[50:51], 0, s[24:25]
	v_lshl_add_u64 v[178:179], v[50:51], 0, s[26:27]
	v_lshl_add_u64 v[176:177], v[50:51], 0, s[28:29]
	v_lshl_add_u64 v[34:35], s[14:15], 0, v[50:51]
	v_lshl_add_u64 v[50:51], v[36:37], 0, v[186:187]
	v_lshl_add_u64 v[52:53], v[36:37], 0, v[184:185]
	v_lshl_add_u64 v[58:59], v[36:37], 0, v[182:183]
	v_lshl_add_u64 v[60:61], v[36:37], 0, v[180:181]
	v_lshl_add_u64 v[236:237], v[36:37], 0, v[178:179]
	v_lshl_add_u64 v[36:37], v[36:37], 0, v[176:177]
	v_lshl_add_u64 v[238:239], v[34:35], 0, v[174:175]
	global_load_dwordx4 v[226:229], v[50:51], off nt
	global_load_dwordx4 v[230:233], v[50:51], off offset:64 nt
	global_load_dwordx4 v[166:169], v[52:53], off nt
	global_load_dwordx4 v[146:149], v[52:53], off offset:64 nt
	global_load_dwordx4 v[134:137], v[58:59], off nt
	global_load_dwordx4 v[122:125], v[58:59], off offset:64 nt
	global_load_dwordx4 v[110:113], v[60:61], off nt
	global_load_dwordx4 v[98:101], v[60:61], off offset:64 nt
	global_load_dwordx4 v[82:85], v[236:237], off nt
	s_nop 0
	global_load_dwordx4 v[58:61], v[236:237], off offset:64 nt
	global_load_dwordx4 v[50:53], v[36:37], off nt
	s_nop 0
	global_load_dwordx4 v[34:37], v[36:37], off offset:64 nt
	s_and_b64 vcc, exec, s[6:7]
	s_mov_b64 s[4:5], -1
	s_waitcnt vmcnt(15)
	v_lshlrev_b32_e32 v236, 16, v210
	v_and_b32_e32 v237, 0xffff0000, v210
	v_lshlrev_b32_e32 v210, 16, v211
	v_and_b32_e32 v211, 0xffff0000, v211
	v_lshlrev_b32_e32 v240, 16, v212
	v_and_b32_e32 v241, 0xffff0000, v212
	v_lshlrev_b32_e32 v212, 16, v213
	v_and_b32_e32 v213, 0xffff0000, v213
	v_pk_add_f32 v[152:153], v[152:153], v[210:211]
	v_pk_add_f32 v[150:151], v[150:151], v[236:237]
	s_waitcnt vmcnt(14)
	v_lshlrev_b32_e32 v242, 16, v214
	v_and_b32_e32 v243, 0xffff0000, v214
	v_lshlrev_b32_e32 v214, 16, v215
	v_and_b32_e32 v215, 0xffff0000, v215
	v_lshlrev_b32_e32 v244, 16, v216
	v_and_b32_e32 v245, 0xffff0000, v216
	v_lshlrev_b32_e32 v216, 16, v217
	v_and_b32_e32 v217, 0xffff0000, v217
	v_pk_add_f32 v[156:157], v[156:157], v[212:213]
	v_pk_add_f32 v[154:155], v[154:155], v[240:241]
	v_cvt_pk_bf16_f32 v150, v150, v151
	v_cvt_pk_bf16_f32 v151, v152, v153
	v_pk_add_f32 v[164:165], v[164:165], v[214:215]
	v_cvt_pk_bf16_f32 v152, v154, v155
	v_cvt_pk_bf16_f32 v153, v156, v157
	v_pk_add_f32 v[162:163], v[162:163], v[242:243]
	v_pk_add_f32 v[160:161], v[160:161], v[216:217]
	v_pk_add_f32 v[158:159], v[158:159], v[244:245]
	s_waitcnt vmcnt(13)
	v_lshlrev_b32_e32 v210, 16, v218
	v_and_b32_e32 v211, 0xffff0000, v218
	global_store_dwordx4 v[238:239], v[150:153], off
	v_pk_add_f32 v[142:143], v[142:143], v[210:211]
	v_lshlrev_b32_e32 v212, 16, v219
	v_cvt_pk_bf16_f32 v150, v162, v163
	v_cvt_pk_bf16_f32 v151, v164, v165
	v_cvt_pk_bf16_f32 v152, v158, v159
	v_cvt_pk_bf16_f32 v153, v160, v161
	global_store_dwordx4 v[238:239], v[150:153], off offset:64
	v_and_b32_e32 v213, 0xffff0000, v219
	v_pk_add_f32 v[144:145], v[144:145], v[212:213]
	v_lshlrev_b32_e32 v150, 16, v220
	v_and_b32_e32 v151, 0xffff0000, v220
	v_lshlrev_b32_e32 v152, 16, v221
	v_and_b32_e32 v153, 0xffff0000, v221
	v_pk_add_f32 v[152:153], v[140:141], v[152:153]
	v_pk_add_f32 v[140:141], v[138:139], v[150:151]
	v_cvt_pk_bf16_f32 v138, v142, v143
	v_lshl_add_u64 v[142:143], s[14:15], 0, v[234:235]
	v_cvt_pk_bf16_f32 v139, v144, v145
	v_cvt_pk_bf16_f32 v140, v140, v141
	v_cvt_pk_bf16_f32 v141, v152, v153
	v_lshl_add_u64 v[142:143], v[142:143], 0, v[174:175]
	global_store_dwordx4 v[142:143], v[138:141], off
	s_waitcnt vmcnt(15)
	s_nop 0
	v_lshlrev_b32_e32 v138, 16, v222
	v_and_b32_e32 v139, 0xffff0000, v222
	v_lshlrev_b32_e32 v140, 16, v223
	v_and_b32_e32 v141, 0xffff0000, v223
	v_pk_add_f32 v[132:133], v[132:133], v[140:141]
	v_pk_add_f32 v[130:131], v[130:131], v[138:139]
	v_lshlrev_b32_e32 v138, 16, v224
	v_and_b32_e32 v139, 0xffff0000, v224
	v_lshlrev_b32_e32 v140, 16, v225
	v_and_b32_e32 v141, 0xffff0000, v225
	v_pk_add_f32 v[140:141], v[128:129], v[140:141]
	v_pk_add_f32 v[128:129], v[126:127], v[138:139]
	v_cvt_pk_bf16_f32 v126, v130, v131
	v_cvt_pk_bf16_f32 v127, v132, v133
	s_nop 0
	v_cvt_pk_bf16_f32 v128, v128, v129
	v_cvt_pk_bf16_f32 v129, v140, v141
	global_store_dwordx4 v[142:143], v[126:129], off offset:64
	s_waitcnt vmcnt(15)
	s_nop 0
	v_lshlrev_b32_e32 v126, 16, v226
	v_and_b32_e32 v127, 0xffff0000, v226
	v_lshlrev_b32_e32 v128, 16, v227
	v_and_b32_e32 v129, 0xffff0000, v227
	v_pk_add_f32 v[120:121], v[120:121], v[128:129]
	v_pk_add_f32 v[118:119], v[118:119], v[126:127]
	v_lshlrev_b32_e32 v126, 16, v228
	v_and_b32_e32 v127, 0xffff0000, v228
	v_lshlrev_b32_e32 v128, 16, v229
	v_and_b32_e32 v129, 0xffff0000, v229
	v_pk_add_f32 v[128:129], v[116:117], v[128:129]
	v_pk_add_f32 v[116:117], v[114:115], v[126:127]
	v_cvt_pk_bf16_f32 v114, v118, v119
	v_lshl_add_u64 v[118:119], s[14:15], 0, v[186:187]
	v_cvt_pk_bf16_f32 v115, v120, v121
	v_cvt_pk_bf16_f32 v116, v116, v117
	v_cvt_pk_bf16_f32 v117, v128, v129
	v_lshl_add_u64 v[118:119], v[118:119], 0, v[174:175]
	global_store_dwordx4 v[118:119], v[114:117], off
	s_waitcnt vmcnt(15)
	s_nop 0
	v_lshlrev_b32_e32 v114, 16, v230
	v_and_b32_e32 v115, 0xffff0000, v230
	v_lshlrev_b32_e32 v116, 16, v231
	v_and_b32_e32 v117, 0xffff0000, v231
	v_pk_add_f32 v[108:109], v[108:109], v[116:117]
	v_pk_add_f32 v[106:107], v[106:107], v[114:115]
	v_lshlrev_b32_e32 v114, 16, v232
	v_and_b32_e32 v115, 0xffff0000, v232
	v_lshlrev_b32_e32 v116, 16, v233
	v_and_b32_e32 v117, 0xffff0000, v233
	v_pk_add_f32 v[116:117], v[104:105], v[116:117]
	v_pk_add_f32 v[104:105], v[102:103], v[114:115]
	v_cvt_pk_bf16_f32 v102, v106, v107
	v_cvt_pk_bf16_f32 v103, v108, v109
	s_nop 0
	v_cvt_pk_bf16_f32 v104, v104, v105
	v_cvt_pk_bf16_f32 v105, v116, v117
	global_store_dwordx4 v[118:119], v[102:105], off offset:64
	s_waitcnt vmcnt(15)
	s_nop 0
	v_lshlrev_b32_e32 v102, 16, v166
	v_and_b32_e32 v103, 0xffff0000, v166
	v_lshlrev_b32_e32 v104, 16, v167
	v_and_b32_e32 v105, 0xffff0000, v167
	v_pk_add_f32 v[96:97], v[96:97], v[104:105]
	v_pk_add_f32 v[94:95], v[94:95], v[102:103]
	v_lshlrev_b32_e32 v102, 16, v168
	v_and_b32_e32 v103, 0xffff0000, v168
	v_lshlrev_b32_e32 v104, 16, v169
	v_and_b32_e32 v105, 0xffff0000, v169
	v_pk_add_f32 v[104:105], v[92:93], v[104:105]
	v_pk_add_f32 v[92:93], v[90:91], v[102:103]
	v_cvt_pk_bf16_f32 v90, v94, v95
	v_lshl_add_u64 v[94:95], s[14:15], 0, v[184:185]
	v_cvt_pk_bf16_f32 v91, v96, v97
	v_cvt_pk_bf16_f32 v92, v92, v93
	v_cvt_pk_bf16_f32 v93, v104, v105
	v_lshl_add_u64 v[94:95], v[94:95], 0, v[174:175]
	global_store_dwordx4 v[94:95], v[90:93], off
	s_waitcnt vmcnt(15)
	s_nop 0
	v_lshlrev_b32_e32 v90, 16, v146
	v_and_b32_e32 v91, 0xffff0000, v146
	v_lshlrev_b32_e32 v92, 16, v147
	v_and_b32_e32 v93, 0xffff0000, v147
	v_pk_add_f32 v[80:81], v[80:81], v[92:93]
	v_pk_add_f32 v[78:79], v[78:79], v[90:91]
	v_lshlrev_b32_e32 v90, 16, v148
	v_and_b32_e32 v91, 0xffff0000, v148
	v_lshlrev_b32_e32 v92, 16, v149
	v_and_b32_e32 v93, 0xffff0000, v149
	v_pk_add_f32 v[92:93], v[72:73], v[92:93]
	v_pk_add_f32 v[72:73], v[70:71], v[90:91]
	v_cvt_pk_bf16_f32 v70, v78, v79
	v_cvt_pk_bf16_f32 v71, v80, v81
	s_waitcnt vmcnt(14)
	v_lshlrev_b32_e32 v78, 16, v136
	v_cvt_pk_bf16_f32 v72, v72, v73
	v_cvt_pk_bf16_f32 v73, v92, v93
	global_store_dwordx4 v[94:95], v[70:73], off offset:64
	v_and_b32_e32 v79, 0xffff0000, v136
	v_pk_add_f32 v[74:75], v[74:75], v[78:79]
	v_lshlrev_b32_e32 v70, 16, v134
	v_and_b32_e32 v71, 0xffff0000, v134
	v_lshlrev_b32_e32 v72, 16, v135
	v_and_b32_e32 v73, 0xffff0000, v135
	v_pk_add_f32 v[72:73], v[88:89], v[72:73]
	v_pk_add_f32 v[70:71], v[86:87], v[70:71]
	v_lshlrev_b32_e32 v80, 16, v137
	v_and_b32_e32 v81, 0xffff0000, v137
	v_cvt_pk_bf16_f32 v70, v70, v71
	v_cvt_pk_bf16_f32 v71, v72, v73
	v_cvt_pk_bf16_f32 v72, v74, v75
	v_lshl_add_u64 v[74:75], s[14:15], 0, v[182:183]
	v_pk_add_f32 v[76:77], v[76:77], v[80:81]
	v_lshl_add_u64 v[74:75], v[74:75], 0, v[174:175]
	v_cvt_pk_bf16_f32 v73, v76, v77
	global_store_dwordx4 v[74:75], v[70:73], off
	s_waitcnt vmcnt(15)
	s_nop 0
	v_lshlrev_b32_e32 v70, 16, v122
	v_and_b32_e32 v71, 0xffff0000, v122
	v_lshlrev_b32_e32 v72, 16, v123
	v_and_b32_e32 v73, 0xffff0000, v123
	v_pk_add_f32 v[68:69], v[68:69], v[72:73]
	v_pk_add_f32 v[66:67], v[66:67], v[70:71]
	v_lshlrev_b32_e32 v70, 16, v124
	v_and_b32_e32 v71, 0xffff0000, v124
	v_lshlrev_b32_e32 v72, 16, v125
	v_and_b32_e32 v73, 0xffff0000, v125
	v_pk_add_f32 v[72:73], v[64:65], v[72:73]
	v_pk_add_f32 v[64:65], v[62:63], v[70:71]
	v_cvt_pk_bf16_f32 v62, v66, v67
	v_cvt_pk_bf16_f32 v63, v68, v69
	s_nop 0
	v_cvt_pk_bf16_f32 v64, v64, v65
	v_cvt_pk_bf16_f32 v65, v72, v73
	global_store_dwordx4 v[74:75], v[62:65], off offset:64
	s_waitcnt vmcnt(15)
	s_nop 0
	v_lshlrev_b32_e32 v62, 16, v110
	v_and_b32_e32 v63, 0xffff0000, v110
	v_lshlrev_b32_e32 v64, 16, v111
	v_and_b32_e32 v65, 0xffff0000, v111
	v_pk_add_f32 v[56:57], v[56:57], v[64:65]
	v_pk_add_f32 v[54:55], v[54:55], v[62:63]
	v_lshlrev_b32_e32 v62, 16, v112
	v_and_b32_e32 v63, 0xffff0000, v112
	v_lshlrev_b32_e32 v64, 16, v113
	v_and_b32_e32 v65, 0xffff0000, v113
	v_pk_add_f32 v[64:65], v[48:49], v[64:65]
	v_pk_add_f32 v[48:49], v[46:47], v[62:63]
	v_cvt_pk_bf16_f32 v46, v54, v55
	v_lshl_add_u64 v[54:55], s[14:15], 0, v[180:181]
	v_cvt_pk_bf16_f32 v47, v56, v57
	v_cvt_pk_bf16_f32 v48, v48, v49
	v_cvt_pk_bf16_f32 v49, v64, v65
	v_lshl_add_u64 v[54:55], v[54:55], 0, v[174:175]
	global_store_dwordx4 v[54:55], v[46:49], off
	s_waitcnt vmcnt(15)
	s_nop 0
	v_lshlrev_b32_e32 v46, 16, v98
	v_and_b32_e32 v47, 0xffff0000, v98
	v_lshlrev_b32_e32 v48, 16, v99
	v_and_b32_e32 v49, 0xffff0000, v99
	v_pk_add_f32 v[44:45], v[44:45], v[48:49]
	v_pk_add_f32 v[42:43], v[42:43], v[46:47]
	v_lshlrev_b32_e32 v46, 16, v100
	v_and_b32_e32 v47, 0xffff0000, v100
	v_lshlrev_b32_e32 v48, 16, v101
	v_and_b32_e32 v49, 0xffff0000, v101
	v_pk_add_f32 v[48:49], v[40:41], v[48:49]
	v_pk_add_f32 v[40:41], v[38:39], v[46:47]
	v_cvt_pk_bf16_f32 v38, v42, v43
	v_cvt_pk_bf16_f32 v39, v44, v45
	s_nop 0
	v_cvt_pk_bf16_f32 v40, v40, v41
	v_cvt_pk_bf16_f32 v41, v48, v49
	global_store_dwordx4 v[54:55], v[38:41], off offset:64
	s_waitcnt vmcnt(15)
	s_nop 0
	v_lshlrev_b32_e32 v38, 16, v82
	v_and_b32_e32 v39, 0xffff0000, v82
	v_lshlrev_b32_e32 v40, 16, v83
	v_and_b32_e32 v41, 0xffff0000, v83
	v_pk_add_f32 v[32:33], v[32:33], v[40:41]
	v_pk_add_f32 v[30:31], v[30:31], v[38:39]
	v_lshlrev_b32_e32 v38, 16, v84
	v_and_b32_e32 v39, 0xffff0000, v84
	v_lshlrev_b32_e32 v40, 16, v85
	v_and_b32_e32 v41, 0xffff0000, v85
	v_pk_add_f32 v[40:41], v[28:29], v[40:41]
	v_pk_add_f32 v[28:29], v[26:27], v[38:39]
	v_cvt_pk_bf16_f32 v26, v30, v31
	v_lshl_add_u64 v[30:31], s[14:15], 0, v[178:179]
	v_cvt_pk_bf16_f32 v27, v32, v33
	v_cvt_pk_bf16_f32 v28, v28, v29
	v_cvt_pk_bf16_f32 v29, v40, v41
	v_lshl_add_u64 v[30:31], v[30:31], 0, v[174:175]
	global_store_dwordx4 v[30:31], v[26:29], off
	s_waitcnt vmcnt(15)
	s_nop 0
	v_lshlrev_b32_e32 v26, 16, v58
	v_and_b32_e32 v27, 0xffff0000, v58
	v_lshlrev_b32_e32 v28, 16, v59
	v_and_b32_e32 v29, 0xffff0000, v59
	v_pk_add_f32 v[24:25], v[24:25], v[28:29]
	v_pk_add_f32 v[22:23], v[22:23], v[26:27]
	v_lshlrev_b32_e32 v26, 16, v60
	v_and_b32_e32 v27, 0xffff0000, v60
	v_lshlrev_b32_e32 v28, 16, v61
	v_and_b32_e32 v29, 0xffff0000, v61
	v_pk_add_f32 v[28:29], v[20:21], v[28:29]
	v_pk_add_f32 v[20:21], v[18:19], v[26:27]
	v_cvt_pk_bf16_f32 v18, v22, v23
	v_cvt_pk_bf16_f32 v19, v24, v25
	s_nop 0
	v_cvt_pk_bf16_f32 v20, v20, v21
	v_cvt_pk_bf16_f32 v21, v28, v29
	global_store_dwordx4 v[30:31], v[18:21], off offset:64
	s_waitcnt vmcnt(15)
	s_nop 0
	v_lshlrev_b32_e32 v18, 16, v50
	v_and_b32_e32 v19, 0xffff0000, v50
	v_lshlrev_b32_e32 v20, 16, v51
	v_and_b32_e32 v21, 0xffff0000, v51
	v_pk_add_f32 v[16:17], v[16:17], v[20:21]
	v_pk_add_f32 v[14:15], v[14:15], v[18:19]
	v_lshlrev_b32_e32 v18, 16, v52
	v_and_b32_e32 v19, 0xffff0000, v52
	v_lshlrev_b32_e32 v20, 16, v53
	v_and_b32_e32 v21, 0xffff0000, v53
	v_pk_add_f32 v[20:21], v[12:13], v[20:21]
	v_pk_add_f32 v[12:13], v[10:11], v[18:19]
	v_cvt_pk_bf16_f32 v10, v14, v15
	v_lshl_add_u64 v[14:15], s[14:15], 0, v[176:177]
	v_cvt_pk_bf16_f32 v11, v16, v17
	v_cvt_pk_bf16_f32 v12, v12, v13
	v_cvt_pk_bf16_f32 v13, v20, v21
	v_lshl_add_u64 v[14:15], v[14:15], 0, v[174:175]
	global_store_dwordx4 v[14:15], v[10:13], off
	s_waitcnt vmcnt(15)
	s_nop 0
	v_lshlrev_b32_e32 v10, 16, v34
	v_and_b32_e32 v11, 0xffff0000, v34
	v_lshlrev_b32_e32 v12, 16, v35
	v_and_b32_e32 v13, 0xffff0000, v35
	v_pk_add_f32 v[8:9], v[8:9], v[12:13]
	v_pk_add_f32 v[6:7], v[6:7], v[10:11]
	v_lshlrev_b32_e32 v10, 16, v36
	v_and_b32_e32 v11, 0xffff0000, v36
	v_lshlrev_b32_e32 v12, 16, v37
	v_and_b32_e32 v13, 0xffff0000, v37
	v_pk_add_f32 v[12:13], v[4:5], v[12:13]
	v_pk_add_f32 v[4:5], v[2:3], v[10:11]
	v_cvt_pk_bf16_f32 v2, v6, v7
	v_cvt_pk_bf16_f32 v3, v8, v9
	s_nop 0
	v_cvt_pk_bf16_f32 v4, v4, v5
	v_cvt_pk_bf16_f32 v5, v12, v13
	global_store_dwordx4 v[14:15], v[2:5], off offset:64
	s_cbranch_vccnz .LBB0_360
	s_andn2_b64 vcc, exec, s[12:13]
	s_cbranch_vccnz .LBB0_359
	s_barrier
	s_branch .LBB0_359

.LBB0_718:
	s_ashr_i32 s7, s6, 31
	s_lshl_b64 s[0:1], s[6:7], 2
	s_add_u32 s0, s16, s0
	s_addc_u32 s1, s17, s1
	global_load_dwordx2 v[28:29], v[20:21], off offset:-1024 nt
	global_load_dwordx2 v[26:27], v[20:21], off offset:-512 nt
	global_load_dwordx2 v[24:25], v[20:21], off nt
	global_load_dwordx2 v[30:31], v[20:21], off offset:-1536 nt
	global_load_dwordx4 v[36:39], v17, s[0:1]
	v_lshl_add_u64 v[20:21], v[20:21], 0, s[10:11]
	s_waitcnt vmcnt(4)
	v_lshlrev_b32_e32 v32, 16, v28
	s_waitcnt vmcnt(3)
	v_lshlrev_b32_e32 v35, 16, v27
	v_and_b32_e32 v46, 0xffff0000, v27
	v_lshlrev_b32_e32 v42, 16, v26
	s_waitcnt vmcnt(0)
	v_readfirstlane_b32 s1, v36
	s_ashr_i32 s18, s1, 16
	v_readfirstlane_b32 s20, v37
	s_and_b32 s22, s1, 0xffff
	s_ashr_i32 s19, s18, 31
	s_lshl_b32 s1, s18, 2
	s_ashr_i32 s0, s20, 16
	s_add_i32 s1, s3, s1
	s_lshl_b64 s[18:19], s[18:19], 18
	s_add_u32 s18, s2, s18
	v_and_b32_e32 v43, 0xffff0000, v26
	v_lshlrev_b32_e32 v26, 16, v24
	v_and_b32_e32 v27, 0xffff0000, v24
	v_mov_b32_e32 v24, s1
	s_addc_u32 s19, s13, s19
	s_lshl_b32 s23, s0, 2
	v_lshlrev_b32_e32 v48, 16, v25
	v_and_b32_e32 v124, 0xffff0000, v25
	ds_read_b32 v25, v24
	s_ashr_i32 s1, s0, 31
	s_and_b32 s24, s20, 0xffff
	s_add_i32 s20, s3, s23
	s_lshl_b32 s21, s22, 2
	s_lshl_b64 s[0:1], s[0:1], 18
	v_mov_b32_e32 v36, s20
	v_readfirstlane_b32 s7, v38
	s_add_u32 s0, s2, s0
	ds_read_b32 v38, v36
	v_mov_b32_e32 v24, s21
	global_load_dword v24, v24, s[18:19]
	s_addc_u32 s1, s13, s1
	s_lshl_b32 s19, s24, 2
	s_ashr_i32 s20, s7, 16
	v_readfirstlane_b32 s15, v39
	v_mov_b32_e32 v37, s19
	s_ashr_i32 s21, s20, 31
	s_lshl_b32 s19, s20, 2
	s_ashr_i32 s18, s15, 16
	s_and_b32 s7, s7, 0xffff
	s_waitcnt lgkmcnt(1)
	v_add_u32_e32 v36, s22, v25
	global_load_dword v25, v37, s[0:1]
	s_add_i32 s19, s3, s19
	s_lshl_b64 s[0:1], s[20:21], 18
	s_add_u32 s0, s2, s0
	v_mov_b32_e32 v39, s19
	s_addc_u32 s1, s13, s1
	s_lshl_b32 s20, s7, 2
	s_lshl_b32 s21, s18, 2
	ds_read_b32 v47, v39
	v_mov_b32_e32 v39, s20
	s_add_i32 s20, s3, s21
	s_ashr_i32 s19, s18, 31
	v_mov_b32_e32 v45, s20
	v_ashrrev_i32_e32 v37, 31, v36
	s_and_b32 s15, s15, 0xffff
	s_waitcnt lgkmcnt(1)
	v_add_u32_e32 v38, s24, v38
	s_lshl_b64 s[18:19], s[18:19], 18
	ds_read_b32 v49, v45
	v_lshlrev_b64 v[36:37], 10, v[36:37]
	global_load_dword v44, v39, s[0:1]
	s_add_u32 s0, s2, s18
	v_ashrrev_i32_e32 v39, 31, v38
	v_lshl_add_u64 v[36:37], v[18:19], 0, v[36:37]
	s_addc_u32 s1, s13, s19
	s_lshl_b32 s18, s15, 2
	v_lshlrev_b64 v[38:39], 10, v[38:39]
	v_mov_b32_e32 v50, s18
	v_lshl_add_u64 v[38:39], v[18:19], 0, v[38:39]
	global_load_dword v53, v[36:37], off nt
	global_load_dword v55, v[36:37], off offset:256 nt
	global_load_dword v56, v[36:37], off offset:512 nt
	global_load_dword v59, v[36:37], off offset:768 nt
	global_load_dword v61, v[38:39], off nt
	global_load_dword v63, v[38:39], off offset:256 nt
	global_load_dword v66, v[38:39], off offset:512 nt
	global_load_dword v76, v[38:39], off offset:768 nt
	global_load_dword v45, v50, s[0:1]
	s_waitcnt lgkmcnt(1)
	v_add_u32_e32 v36, s7, v47
	v_ashrrev_i32_e32 v37, 31, v36
	v_lshlrev_b64 v[36:37], 10, v[36:37]
	s_waitcnt lgkmcnt(0)
	v_add_u32_e32 v38, s15, v49
	v_lshl_add_u64 v[36:37], v[18:19], 0, v[36:37]
	v_ashrrev_i32_e32 v39, 31, v38
	global_load_dword v82, v[36:37], off nt
	global_load_dword v84, v[36:37], off offset:256 nt
	global_load_dword v86, v[36:37], off offset:512 nt
	global_load_dword v88, v[36:37], off offset:768 nt
	v_lshlrev_b64 v[36:37], 10, v[38:39]
	v_lshl_add_u64 v[36:37], v[18:19], 0, v[36:37]
	global_load_dword v38, v[36:37], off nt
	global_load_dword v90, v[36:37], off offset:256 nt
	global_load_dword v92, v[36:37], off offset:512 nt
	global_load_dword v94, v[36:37], off offset:768 nt
	v_lshlrev_b32_e32 v40, 16, v30
	v_and_b32_e32 v41, 0xffff0000, v30
	v_and_b32_e32 v33, 0xffff0000, v28
	v_lshlrev_b32_e32 v30, 16, v31
	v_and_b32_e32 v31, 0xffff0000, v31
	v_lshlrev_b32_e32 v28, 16, v29
	v_and_b32_e32 v29, 0xffff0000, v29
	s_add_i32 s4, s4, s80
	s_add_i32 s6, s6, s14
	s_cmp_gt_i32 s4, 0xffff
	s_waitcnt vmcnt(18)
	v_pk_mul_f32 v[24:25], v[24:25], s[12:13] op_sel_hi:[1,0]
	s_nop 0
	v_mov_b32_e32 v37, v24
	v_mov_b32_e32 v47, v24
	v_mov_b32_e32 v49, v24
	v_mov_b32_e32 v39, v25
	s_waitcnt vmcnt(16)
	v_cvt_f32_fp8_e32 v50, v53
	s_waitcnt vmcnt(15)
	v_cvt_f32_fp8_sdwa v58, v55 src0_sel:BYTE_2
	v_cvt_f32_fp8_sdwa v60, v55 src0_sel:BYTE_3
	s_waitcnt vmcnt(13)
	v_cvt_f32_fp8_e32 v70, v59
	v_cvt_f32_fp8_sdwa v72, v59 src0_sel:BYTE_1
	v_cvt_f32_fp8_sdwa v74, v59 src0_sel:BYTE_2
	v_cvt_f32_fp8_sdwa v77, v59 src0_sel:BYTE_3
	s_waitcnt vmcnt(12)
	v_cvt_f32_fp8_e32 v78, v61
	v_cvt_f32_fp8_sdwa v79, v61 src0_sel:BYTE_1
	v_cvt_f32_fp8_sdwa v80, v61 src0_sel:BYTE_2
	v_cvt_f32_fp8_sdwa v81, v61 src0_sel:BYTE_3
	s_waitcnt vmcnt(11)
	v_cvt_f32_fp8_sdwa v59, v63 src0_sel:BYTE_2
	v_cvt_f32_fp8_sdwa v61, v63 src0_sel:BYTE_3
	v_cvt_f32_fp8_sdwa v51, v53 src0_sel:BYTE_1
	v_cvt_f32_fp8_e32 v54, v55
	v_cvt_f32_fp8_sdwa v57, v55 src0_sel:BYTE_1
	v_cvt_f32_fp8_e32 v62, v56
	v_cvt_f32_fp8_sdwa v64, v56 src0_sel:BYTE_1
	v_cvt_f32_fp8_e32 v55, v63
	v_cvt_f32_fp8_sdwa v83, v63 src0_sel:BYTE_1
	s_waitcnt vmcnt(10)
	v_cvt_f32_fp8_e32 v63, v66
	v_cvt_f32_fp8_sdwa v65, v66 src0_sel:BYTE_1
	v_cvt_f32_fp8_sdwa v52, v53 src0_sel:BYTE_2
	v_cvt_f32_fp8_sdwa v53, v53 src0_sel:BYTE_3
	v_cvt_f32_fp8_sdwa v68, v56 src0_sel:BYTE_3
	v_cvt_f32_fp8_sdwa v69, v66 src0_sel:BYTE_3
	s_waitcnt vmcnt(9)
	v_cvt_f32_fp8_sdwa v75, v76 src0_sel:BYTE_2
	v_pk_mul_f32 v[58:59], v[24:25], v[58:59]
	v_pk_mul_f32 v[60:61], v[24:25], v[60:61]
	v_pk_mul_f32 v[64:65], v[24:25], v[64:65]
	v_pk_mul_f32 v[62:63], v[24:25], v[62:63]
	s_waitcnt vmcnt(7)
	v_cvt_f32_fp8_e32 v96, v82
	v_cvt_f32_fp8_sdwa v97, v82 src0_sel:BYTE_1
	v_pk_fma_f32 v[40:41], v[24:25], v[50:51], v[40:41] op_sel_hi:[0,1,1]
	v_mov_b32_e32 v50, v58
	v_mov_b32_e32 v51, v60
	v_cvt_f32_fp8_e32 v71, v76
	v_cvt_f32_fp8_sdwa v73, v76 src0_sel:BYTE_1
	v_cvt_f32_fp8_sdwa v98, v82 src0_sel:BYTE_2
	v_cvt_f32_fp8_sdwa v99, v82 src0_sel:BYTE_3
	s_waitcnt vmcnt(5)
	v_cvt_f32_fp8_sdwa v114, v86 src0_sel:BYTE_3
	s_waitcnt vmcnt(4)
	v_cvt_f32_fp8_sdwa v120, v88 src0_sel:BYTE_2
	v_pk_fma_f32 v[30:31], v[24:25], v[52:53], v[30:31] op_sel_hi:[0,1,1]
	v_mov_b32_e32 v52, v62
	v_mov_b32_e32 v53, v64
	v_pk_add_f32 v[28:29], v[50:51], v[28:29]
	s_waitcnt vmcnt(3)
	v_cvt_f32_fp8_e32 v50, v38
	v_cvt_f32_fp8_sdwa v51, v38 src0_sel:BYTE_1
	s_waitcnt vmcnt(1)
	v_cvt_f32_fp8_sdwa v115, v92 src0_sel:BYTE_3
	s_waitcnt vmcnt(0)
	v_cvt_f32_fp8_sdwa v121, v94 src0_sel:BYTE_2
	v_cvt_f32_fp8_e32 v100, v84
	v_pk_add_f32 v[42:43], v[52:53], v[42:43]
	v_cvt_f32_fp8_sdwa v52, v38 src0_sel:BYTE_2
	v_cvt_f32_fp8_sdwa v53, v38 src0_sel:BYTE_3
	v_cvt_f32_fp8_e32 v101, v90
	v_pk_mul_f32 v[44:45], v[44:45], s[12:13] op_sel_hi:[1,0]
	v_pk_mul_f32 v[54:55], v[24:25], v[54:55]
	v_pk_mul_f32 v[68:69], v[24:25], v[68:69]
	v_pk_mul_f32 v[74:75], v[24:25], v[74:75]
	v_pk_fma_f32 v[40:41], v[24:25], v[78:79], v[40:41] op_sel:[1,0,0]
	v_add_f32_e32 v32, v54, v32
	v_add_f32_e32 v36, v68, v46
	v_add_f32_e32 v46, v74, v48
	v_pk_fma_f32 v[30:31], v[24:25], v[80:81], v[30:31] op_sel:[1,0,0]
	v_pk_fma_f32 v[40:41], v[44:45], v[96:97], v[40:41] op_sel_hi:[0,1,1]
	v_pk_mul_f32 v[70:71], v[24:25], v[70:71]
	v_pk_mul_f32 v[72:73], v[24:25], v[72:73]
	v_cvt_f32_fp8_sdwa v103, v84 src0_sel:BYTE_1
	v_cvt_f32_fp8_sdwa v104, v84 src0_sel:BYTE_2
	v_cvt_f32_fp8_sdwa v106, v84 src0_sel:BYTE_3
	v_mov_b32_e32 v64, v63
	v_add_f32_e32 v24, v32, v55
	v_add_f32_e32 v32, v36, v69
	v_add_f32_e32 v36, v46, v75
	v_cvt_f32_fp8_sdwa v105, v90 src0_sel:BYTE_2
	v_cvt_f32_fp8_sdwa v107, v90 src0_sel:BYTE_3
	v_pk_fma_f32 v[30:31], v[44:45], v[98:99], v[30:31] op_sel_hi:[0,1,1]
	v_pk_mul_f32 v[74:75], v[44:45], v[114:115]
	v_pk_mul_f32 v[96:97], v[44:45], v[120:121]
	v_pk_fma_f32 v[40:41], v[44:45], v[50:51], v[40:41] op_sel:[1,0,0]
	v_cvt_f32_fp8_sdwa v67, v56 src0_sel:BYTE_2
	v_cvt_f32_fp8_sdwa v55, v90 src0_sel:BYTE_1
	v_pk_add_f32 v[42:43], v[42:43], v[64:65]
	v_pk_mul_f32 v[64:65], v[44:45], v[100:101]
	v_pk_fma_f32 v[30:31], v[44:45], v[52:53], v[30:31] op_sel:[1,0,0]
	v_add_f32_e32 v46, v32, v74
	v_add_f32_e32 v48, v36, v96
	v_mov_b32_e32 v36, v40
	v_mov_b32_e32 v56, v40
	v_mul_f32_e32 v32, v41, v41
	v_cvt_f32_fp8_e32 v108, v86
	v_cvt_f32_fp8_sdwa v110, v86 src0_sel:BYTE_1
	v_cvt_f32_fp8_e32 v109, v92
	v_cvt_f32_fp8_sdwa v111, v92 src0_sel:BYTE_1
	v_add_f32_e32 v24, v24, v64
	v_mov_b32_e32 v38, v30
	v_mov_b32_e32 v82, v30
	v_pk_fma_f32 v[32:33], v[36:37], v[56:57], v[32:33]
	v_cvt_f32_fp8_e32 v116, v88
	v_cvt_f32_fp8_sdwa v118, v88 src0_sel:BYTE_1
	v_cvt_f32_fp8_sdwa v123, v88 src0_sel:BYTE_3
	v_pk_mov_b32 v[50:51], v[30:31], v[44:45] op_sel:[1,0]
	v_mov_b32_e32 v102, v31
	v_add_f32_e32 v88, v24, v65
	v_pk_fma_f32 v[32:33], v[38:39], v[82:83], v[32:33]
	v_mov_b32_e32 v89, v45
	v_mov_b32_e32 v60, v59
	v_mov_b32_e32 v58, v70
	v_mov_b32_e32 v59, v72
	v_mov_b32_e32 v72, v71
	v_pk_mul_f32 v[68:69], v[44:45], v[104:105]
	v_pk_mul_f32 v[70:71], v[44:45], v[106:107]
	v_mov_b32_e32 v54, v88
	v_pk_fma_f32 v[32:33], v[50:51], v[102:103], v[32:33]
	v_pk_add_f32 v[26:27], v[58:59], v[26:27]
	v_cvt_f32_fp8_e32 v117, v94
	v_cvt_f32_fp8_sdwa v119, v94 src0_sel:BYTE_1
	v_pk_add_f32 v[28:29], v[28:29], v[60:61]
	v_mov_b32_e32 v52, v68
	v_mov_b32_e32 v53, v70
	v_add_f32_e32 v46, v46, v75
	v_pk_fma_f32 v[32:33], v[88:89], v[54:55], v[32:33]
	v_cvt_f32_fp8_sdwa v85, v66 src0_sel:BYTE_2
	v_pk_add_f32 v[26:27], v[26:27], v[72:73]
	v_pk_mul_f32 v[60:61], v[44:45], v[110:111]
	v_pk_mul_f32 v[72:73], v[44:45], v[108:109]
	v_mov_b32_e32 v70, v69
	v_pk_add_f32 v[28:29], v[28:29], v[52:53]
	v_mov_b32_e32 v39, v46
	v_mul_f32_e32 v38, v33, v33
	v_cvt_f32_fp8_sdwa v113, v86 src0_sel:BYTE_2
	v_mov_b32_e32 v68, v72
	v_mov_b32_e32 v69, v60
	v_pk_add_f32 v[28:29], v[28:29], v[70:71]
	v_mov_b32_e32 v89, v33
	v_pk_add_f32 v[32:33], v[32:33], v[38:39] op_sel_hi:[1,0]
	v_cvt_f32_fp8_sdwa v59, v92 src0_sel:BYTE_2
	v_mov_b32_e32 v60, v73
	v_add_f32_e32 v90, v48, v97
	v_pk_add_f32 v[36:37], v[42:43], v[68:69]
	v_mov_b32_e32 v48, v28
	v_mov_b32_e32 v66, v28
	v_mov_b32_e32 v33, v35
	v_pk_mul_f32 v[78:79], v[44:45], v[116:117]
	v_pk_mul_f32 v[80:81], v[44:45], v[118:119]
	v_pk_add_f32 v[36:37], v[36:37], v[60:61]
	v_mov_b32_e32 v24, v29
	v_mov_b32_e32 v84, v29
	v_pk_fma_f32 v[32:33], v[48:49], v[66:67], v[32:33]
	v_mov_b32_e32 v93, v44
	v_mov_b32_e32 v72, v78
	v_mov_b32_e32 v73, v80
	v_mov_b32_e32 v92, v36
	v_mov_b32_e32 v112, v36
	v_pk_fma_f32 v[32:33], v[24:25], v[84:85], v[32:33]
	v_mov_b32_e32 v95, v45
	v_cvt_f32_fp8_sdwa v63, v94 src0_sel:BYTE_3
	v_mov_b32_e32 v80, v79
	v_pk_add_f32 v[26:27], v[26:27], v[72:73]
	v_mov_b32_e32 v94, v37
	v_mov_b32_e32 v58, v37
	v_pk_fma_f32 v[32:33], v[92:93], v[112:113], v[32:33]
	v_pk_add_f32 v[26:27], v[26:27], v[80:81]
	v_pk_fma_f32 v[32:33], v[94:95], v[58:59], v[32:33]
	v_cvt_f32_fp8_sdwa v87, v76 src0_sel:BYTE_3
	v_pk_mov_b32 v[42:43], v[26:27], v[44:45] op_sel:[1,0]
	v_mul_f32_e32 v44, v33, v33
	v_mov_b32_e32 v38, v33
	v_pk_add_f32 v[32:33], v[32:33], v[44:45] op_sel_hi:[1,0]
	v_mov_b32_e32 v76, v46
	v_mov_b32_e32 v33, v124
	v_mov_b32_e32 v86, v26
	v_mov_b32_e32 v24, v26
	v_pk_fma_f32 v[32:33], v[46:47], v[76:77], v[32:33]
	v_mov_b32_e32 v122, v42
	v_pk_fma_f32 v[24:25], v[24:25], v[86:87], v[32:33]
	v_mov_b32_e32 v91, v45
	v_mov_b32_e32 v62, v90
	v_pk_fma_f32 v[24:25], v[42:43], v[122:123], v[24:25]
	s_nop 0
	v_pk_fma_f32 v[24:25], v[90:91], v[62:63], v[24:25]
	s_nop 0
	v_fma_f32 v24, v25, v25, v24
	v_mov_b32_e32 v91, v25
	ds_bpermute_b32 v25, v188, v24
	s_waitcnt lgkmcnt(0)
	v_add_f32_e32 v24, v24, v25
	ds_bpermute_b32 v25, v189, v24
	s_waitcnt lgkmcnt(0)
	v_add_f32_e32 v24, v24, v25
	ds_bpermute_b32 v25, v190, v24
	s_waitcnt lgkmcnt(0)
	v_add_f32_e32 v24, v24, v25
	ds_bpermute_b32 v25, v191, v24
	s_waitcnt lgkmcnt(0)
	v_add_f32_e32 v24, v24, v25
	ds_bpermute_b32 v25, v192, v24
	s_waitcnt lgkmcnt(0)
	v_add_f32_e32 v24, v24, v25
	ds_bpermute_b32 v25, v193, v24
	s_waitcnt lgkmcnt(0)
	v_add_f32_e32 v24, v24, v25
	v_fmamk_f32 v24, v24, 0x3a800000, v16
	v_mul_f32_e32 v25, 0x4f800000, v24
	v_cmp_gt_f32_e32 vcc, s5, v24
	s_nop 1
	v_cndmask_b32_e32 v24, v24, v25, vcc
	v_sqrt_f32_e32 v25, v24
	s_nop 0
	v_add_u32_e32 v32, -1, v25
	v_add_u32_e32 v33, 1, v25
	v_fma_f32 v35, -v32, v25, v24
	v_fma_f32 v42, -v33, v25, v24
	v_cmp_ge_f32_e64 s[0:1], 0, v35
	s_nop 1
	v_cndmask_b32_e64 v25, v25, v32, s[0:1]
	v_cmp_lt_f32_e64 s[0:1], 0, v42
	s_nop 1
	v_cndmask_b32_e64 v25, v25, v33, s[0:1]
	v_mul_f32_e32 v32, 0x37800000, v25
	v_cndmask_b32_e32 v25, v25, v32, vcc
	v_cmp_class_f32_e32 vcc, v24, v34
	s_nop 1
	v_cndmask_b32_e32 v24, v25, v24, vcc
	v_div_scale_f32 v25, s[0:1], v24, v24, 1.0
	v_rcp_f32_e32 v33, v25
	v_div_scale_f32 v32, vcc, 1.0, v24, 1.0
	v_fma_f32 v35, -v25, v33, 1.0
	v_fmac_f32_e32 v33, v35, v33
	v_mul_f32_e32 v35, v32, v33
	v_fma_f32 v42, -v25, v35, v32
	v_fmac_f32_e32 v35, v42, v33
	v_fma_f32 v25, -v25, v35, v32
	v_div_fmas_f32 v25, v25, v33, v35
	v_div_fixup_f32 v24, v25, v24, 1.0
	v_pk_mul_f32 v[32:33], v[40:41], v[24:25] op_sel_hi:[1,0]
	v_pk_mul_f32 v[30:31], v[30:31], v[24:25] op_sel_hi:[1,0]
	v_pk_mul_f32 v[40:41], v[88:89], v[24:25] op_sel_hi:[1,0]
	v_pk_mul_f32 v[28:29], v[28:29], v[24:25] op_sel_hi:[1,0]
	v_pk_mul_f32 v[36:37], v[36:37], v[24:25] op_sel_hi:[1,0]
	v_pk_mul_f32 v[38:39], v[38:39], v[24:25] op_sel_hi:[1,0]
	v_pk_mul_f32 v[44:45], v[26:27], v[24:25] op_sel_hi:[1,0]
	v_pk_mul_f32 v[42:43], v[90:91], v[24:25] op_sel_hi:[1,0]
	v_pk_mul_f32 v[26:27], v[2:3], v[30:31]
	v_pk_mul_f32 v[24:25], v[0:1], v[32:33]
	v_pk_mul_f32 v[30:31], v[6:7], v[28:29]
	v_pk_mul_f32 v[28:29], v[4:5], v[40:41]
	v_pk_mul_f32 v[38:39], v[10:11], v[38:39]
	v_pk_mul_f32 v[36:37], v[8:9], v[36:37]
	v_pk_mul_f32 v[42:43], v[14:15], v[42:43]
	v_pk_mul_f32 v[40:41], v[12:13], v[44:45]
	global_store_dwordx4 v[22:23], v[24:27], off offset:-2048
	global_store_dwordx4 v[22:23], v[28:31], off offset:-1024
	global_store_dwordx4 v[22:23], v[36:39], off
	global_store_dwordx4 v[22:23], v[40:43], off offset:1024
	v_lshl_add_u64 v[22:23], v[22:23], 0, s[8:9]
	s_cbranch_scc0 .LBB0_718
